# baseline (speedup 1.0000x reference)
_Z2kA5AArgs:
	s_load_dwordx2 s[34:35], s[0:1], 0x20
	s_load_dwordx16 s[16:31], s[0:1], 0x30
	s_lshl_b32 s3, s2, 3
	v_readfirstlane_b32 s38, v0
	s_and_b32 s3, s3, 56
	s_ashr_i32 s4, s2, 5
	s_lshr_b32 s36, s38, 6
	s_add_i32 s3, s3, s4
	s_bfe_u32 s33, s2, 0x20003
	s_cmp_eq_u32 s33, 0
	s_cbranch_scc1 .Lstag_done
	s_sleep 12
